# attention main loop head aligned to 64 bytes (s_nop padding), otherwise v56
# speedup vs baseline: 1.0043x; 1.0043x over previous
.LBB0_831:
	v_max3_f32 v33, v0, v1, v16
	v_max3_f32 v34, v2, v3, v17
	s_and_b32 s2, s25, 0x3fffffc0
	v_max3_f32 v33, v33, v18, v19
	v_max3_f32 v34, v34, v6, v7
	s_lshl_b32 s2, s2, 2
	v_max3_f32 v33, v33, v4, v5
	v_max3_f32 v34, v34, v22, v23
	s_add_i32 s51, s2, 0
	v_max3_f32 v33, v33, v20, v21
	v_max3_f32 v34, v34, v10, v11
	s_add_u32 s2, s18, 0x18000
	v_max3_f32 v33, v33, v8, v9
	v_max3_f32 v34, v34, v26, v27
	s_addc_u32 s3, s19, 0
	v_max3_f32 v33, v33, v24, v25
	v_max3_f32 v34, v34, v14, v15
	s_mov_b32 s29, 0
	v_max3_f32 v33, v33, v12, v13
	v_max3_f32 v34, v34, v30, v31
	v_lshl_add_u32 v245, v198, 2, s51
	v_max3_f32 v33, v33, v28, v29
	s_nop 0
	v_max_f32_e32 v33, v33, v34
	s_nop 0
	v_mov_b32_e32 v34, v33
	s_nop 1
	v_permlane32_swap_b32_e32 v33, v34
	v_max_f32_e32 v33, v33, v34
	s_nop 0
	v_sub_f32_e32 v0, v0, v33
	v_sub_f32_e32 v16, v16, v33
	v_sub_f32_e32 v1, v1, v33
	v_sub_f32_e32 v17, v17, v33
	v_sub_f32_e32 v2, v2, v33
	v_sub_f32_e32 v18, v18, v33
	v_sub_f32_e32 v3, v3, v33
	v_sub_f32_e32 v19, v19, v33
	v_sub_f32_e32 v4, v4, v33
	v_sub_f32_e32 v20, v20, v33
	v_sub_f32_e32 v5, v5, v33
	v_sub_f32_e32 v21, v21, v33
	v_sub_f32_e32 v6, v6, v33
	v_sub_f32_e32 v22, v22, v33
	v_sub_f32_e32 v7, v7, v33
	v_sub_f32_e32 v23, v23, v33
	v_sub_f32_e32 v8, v8, v33
	v_sub_f32_e32 v24, v24, v33
	v_sub_f32_e32 v9, v9, v33
	v_sub_f32_e32 v25, v25, v33
	v_sub_f32_e32 v10, v10, v33
	v_sub_f32_e32 v26, v26, v33
	v_sub_f32_e32 v11, v11, v33
	v_sub_f32_e32 v27, v27, v33
	v_sub_f32_e32 v12, v12, v33
	v_sub_f32_e32 v28, v28, v33
	v_sub_f32_e32 v13, v13, v33
	v_sub_f32_e32 v29, v29, v33
	v_sub_f32_e32 v14, v14, v33
	v_sub_f32_e32 v30, v30, v33
	v_sub_f32_e32 v15, v15, v33
	v_sub_f32_e32 v31, v31, v33
	s_nop 0
	v_exp_f32_e32 v80, v0
	v_exp_f32_e32 v81, v1
	v_exp_f32_e32 v82, v2
	v_exp_f32_e32 v83, v3
	v_exp_f32_e32 v84, v4
	v_exp_f32_e32 v85, v5
	v_exp_f32_e32 v86, v6
	v_exp_f32_e32 v87, v7
	v_exp_f32_e32 v88, v8
	v_exp_f32_e32 v89, v9
	v_exp_f32_e32 v90, v10
	v_exp_f32_e32 v91, v11
	v_exp_f32_e32 v92, v12
	v_exp_f32_e32 v93, v13
	v_exp_f32_e32 v94, v14
	v_exp_f32_e32 v95, v15
	v_exp_f32_e32 v64, v16
	v_exp_f32_e32 v65, v17
	v_exp_f32_e32 v66, v18
	v_exp_f32_e32 v67, v19
	v_exp_f32_e32 v68, v20
	v_exp_f32_e32 v69, v21
	v_exp_f32_e32 v70, v22
	v_exp_f32_e32 v71, v23
	v_exp_f32_e32 v72, v24
	v_exp_f32_e32 v73, v25
	v_exp_f32_e32 v74, v26
	v_exp_f32_e32 v75, v27
	v_exp_f32_e32 v76, v28
	v_exp_f32_e32 v77, v29
	v_exp_f32_e32 v78, v30
	v_exp_f32_e32 v79, v31
	ds_read_b128 v[0:3], v214 offset:256
	ds_read_b128 v[4:7], v214 offset:288
	ds_read_b128 v[8:11], v214 offset:320
	ds_read_b128 v[12:15], v214 offset:352
	ds_read_b128 v[16:19], v214 offset:384
	ds_read_b128 v[20:23], v214 offset:416
	ds_read_b128 v[24:27], v214 offset:448
	ds_read_b128 v[28:31], v214 offset:480
	s_waitcnt vmcnt(0) lgkmcnt(0)
	s_barrier
	s_mov_b32 m0, s53
	s_nop 0
	global_load_lds_dwordx4 v247, s[2:3]
	s_add_u32 s2, s20, 0x8000
	s_addc_u32 s3, s21, 0
	s_cmp_lg_u32 0, -1
	s_cselect_b32 s23, 0, 0
	s_add_i32 s22, s23, s22
	s_add_i32 s22, s22, 0x8000
	s_mov_b32 m0, s22
	s_nop 0
	global_load_lds_dwordx4 v248, s[2:3]
	ds_read_b128 v[158:161], v213 offset:8192
	ds_read_b128 v[154:157], v213 offset:8704
	ds_read_b128 v[150:153], v213 offset:10240
	ds_read_b128 v[146:149], v213 offset:10752
	ds_read_b128 v[142:145], v213 offset:12288
	ds_read_b128 v[138:141], v213 offset:12800
	ds_read_b128 v[134:137], v213 offset:14336
	ds_read_b128 v[130:133], v213 offset:14848
	s_waitcnt vmcnt(2) lgkmcnt(0)
	s_barrier
	v_add_f32_e32 v244, v97, v33
	v_sub_f32_e32 v249, v32, v33
	s_cmp_lt_i32 s52, 7
	s_waitcnt lgkmcnt(12)
	v_sub_f32_e32 v63, v249, v15
	v_sub_f32_e32 v62, v249, v14
	v_sub_f32_e32 v61, v249, v13
	v_sub_f32_e32 v60, v249, v12
	v_sub_f32_e32 v59, v249, v11
	v_sub_f32_e32 v58, v249, v10
	v_sub_f32_e32 v57, v249, v9
	v_sub_f32_e32 v56, v249, v8
	v_sub_f32_e32 v55, v249, v7
	v_sub_f32_e32 v54, v249, v6
	v_sub_f32_e32 v53, v249, v5
	v_sub_f32_e32 v52, v249, v4
	v_sub_f32_e32 v51, v249, v3
	v_sub_f32_e32 v50, v249, v2
	v_sub_f32_e32 v49, v249, v1
	v_sub_f32_e32 v48, v249, v0
	s_waitcnt lgkmcnt(8)
	v_sub_f32_e32 v47, v249, v31
	v_sub_f32_e32 v46, v249, v30
	v_sub_f32_e32 v45, v249, v29
	v_sub_f32_e32 v44, v249, v28
	v_sub_f32_e32 v43, v249, v27
	v_sub_f32_e32 v42, v249, v26
	v_sub_f32_e32 v41, v249, v25
	v_sub_f32_e32 v40, v249, v24
	v_sub_f32_e32 v39, v249, v23
	v_sub_f32_e32 v38, v249, v22
	v_sub_f32_e32 v37, v249, v21
	v_sub_f32_e32 v36, v249, v20
	v_sub_f32_e32 v35, v249, v19
	v_sub_f32_e32 v34, v249, v18
	v_sub_f32_e32 v33, v249, v17
	v_sub_f32_e32 v32, v249, v16
	s_cbranch_scc1 .LBB0_847
	s_add_u32 s2, s20, 0x18000
	s_addc_u32 s3, s21, 0
	v_mov_b32_e32 v16, v97
	v_mov_b32_e32 v17, v97
	s_add_u32 s22, s18, 0x28000
	v_mov_b32_e32 v18, v97
	v_mov_b32_e32 v19, v97
	v_mov_b32_e32 v20, v97
	v_mov_b32_e32 v21, v97
	v_mov_b32_e32 v22, v97
	v_mov_b32_e32 v23, v97
	v_mov_b32_e32 v24, v97
	v_mov_b32_e32 v25, v97
	v_mov_b32_e32 v26, v97
	v_mov_b32_e32 v27, v97
	v_mov_b32_e32 v28, v97
	v_mov_b32_e32 v29, v97
	v_mov_b32_e32 v30, v97
	v_mov_b32_e32 v31, v97
	v_mov_b64_e32 v[0:1], v[16:17]
	s_addc_u32 s23, s19, 0
	s_mov_b32 s24, 0
	s_movk_i32 s29, 0x4000
	s_movk_i32 s58, 0x2000
	v_mov_b32_e32 v250, 0
	s_mov_b32 s57, 6
	v_mov_b32_e32 v166, v221
	v_mov_b64_e32 v[2:3], v[18:19]
	v_mov_b64_e32 v[4:5], v[20:21]
	v_mov_b64_e32 v[6:7], v[22:23]
	v_mov_b64_e32 v[8:9], v[24:25]
	v_mov_b64_e32 v[10:11], v[26:27]
	v_mov_b64_e32 v[12:13], v[28:29]
	v_mov_b64_e32 v[14:15], v[30:31]
	.p2alignl 6, 3212836864
